# grid barrier: waiters poll the XCD-arrival counter against (generation+1)*nXCD; the separate generation word, its increment by the last arriver and that increment's completion wait are gone
# baseline (speedup 1.0000x reference)
.LBB0_66:
	v_readlane_b32 s0, v254, 6
	s_lshl_b32 s0, s0, 8
	v_readlane_b32 s2, v254, 4
	v_readlane_b32 s3, v254, 5
	s_add_u32 s6, s2, s0
	s_addc_u32 s7, s3, 0
	v_mov_b32_e32 v1, 0x1000
	v_mov_b32_e32 v3, 1
	global_atomic_add v3, v1, v3, s[6:7] offset:1024 sc0
	v_cvt_f32_u32_e32 v1, v2
	v_sub_u32_e32 v4, 0, v2
	v_rcp_iflag_f32_e32 v1, v1
	s_nop 0
	v_mul_f32_e32 v1, 0x4f7ffffe, v1
	v_cvt_u32_f32_e32 v1, v1
	v_mul_lo_u32 v4, v4, v1
	v_mul_hi_u32 v4, v1, v4
	v_add_u32_e32 v1, v1, v4
	s_waitcnt vmcnt(0)
	v_mul_hi_u32 v1, v3, v1
	v_mul_lo_u32 v4, v1, v2
	v_sub_u32_e32 v4, v3, v4
	v_add_u32_e32 v5, 1, v1
	v_cmp_ge_u32_e32 vcc, v4, v2
	v_add_u32_e32 v3, 1, v3
	s_nop 0
	v_cndmask_b32_e32 v1, v1, v5, vcc
	v_sub_u32_e32 v5, v4, v2
	v_cndmask_b32_e32 v4, v4, v5, vcc
	v_add_u32_e32 v5, 1, v1
	v_cmp_ge_u32_e32 vcc, v4, v2
	s_nop 1
	v_cndmask_b32_e32 v1, v1, v5, vcc
	v_mul_lo_u32 v4, v2, v1
	v_add_u32_e32 v2, v4, v2
	v_cmp_ne_u32_e32 vcc, v3, v2
	s_and_saveexec_b64 s[0:1], vcc
	s_xor_b64 s[8:9], exec, s[0:1]
	s_cbranch_execz .LBB0_80
	s_waitcnt lgkmcnt(0)
	s_add_u32 s14, s26, 0x7400
	s_addc_u32 s15, s27, 0
	v_add_u32_e32 v1, 1, v1
	v_mul_lo_u32 v1, v1, v0
	v_mov_b32_e32 v0, 0
	global_load_dword v0, v0, s[14:15] sc1
	s_waitcnt vmcnt(0)
	v_cmp_lt_u32_e32 vcc, v0, v1
	s_and_saveexec_b64 s[10:11], vcc
	s_cbranch_execz .LBB0_79
	s_add_u32 s12, s26, 0x4200
	s_addc_u32 s13, s27, 0
	s_mov_b32 s0, 1
	s_mov_b64 s[16:17], 0
	v_mov_b32_e32 v0, 0
	s_branch .LBB0_70

.LBB0_72:
	global_load_dword v2, v0, s[14:15] sc1
	s_add_i32 s0, s0, 1
	s_mov_b64 s[22:23], -1
	s_waitcnt vmcnt(0)
	v_cmp_ge_u32_e32 vcc, v2, v1
	s_orn2_b64 s[20:21], vcc, exec
	s_branch .LBB0_69

.LBB0_83:
	s_or_b64 exec, exec, s[10:11]
	v_cvt_f32_u32_e32 v3, v0
	s_waitcnt vmcnt(0)
	v_readfirstlane_b32 s0, v2
	s_add_u32 s10, s26, 0x7500
	s_addc_u32 s11, s27, 0
	v_rcp_iflag_f32_e32 v3, v3
	v_add_u32_e32 v1, s0, v1
	v_add_u32_e32 v4, 1, v1
	s_mov_b64 s[12:13], -1
	v_mul_f32_e32 v2, 0x4f7ffffe, v3
	v_cvt_u32_f32_e32 v2, v2
	v_sub_u32_e32 v3, 0, v0
	v_mul_lo_u32 v3, v3, v2
	v_mul_hi_u32 v3, v2, v3
	v_add_u32_e32 v2, v2, v3
	v_mul_hi_u32 v2, v1, v2
	v_mul_lo_u32 v3, v2, v0
	v_sub_u32_e32 v1, v1, v3
	v_add_u32_e32 v5, 1, v2
	v_cmp_ge_u32_e32 vcc, v1, v0
	v_sub_u32_e32 v3, v1, v0
	s_nop 0
	v_cndmask_b32_e32 v2, v2, v5, vcc
	v_cndmask_b32_e32 v1, v1, v3, vcc
	v_add_u32_e32 v3, 1, v2
	v_cmp_ge_u32_e32 vcc, v1, v0
	s_nop 1
	v_cndmask_b32_e32 v2, v2, v3, vcc
	v_mul_lo_u32 v1, v0, v2
	v_add_u32_e32 v0, v1, v0
	v_cmp_ne_u32_e32 vcc, v4, v0
	v_mov_b32_e32 v3, v0
	v_mov_b64_e32 v[0:1], s[10:11]
	s_and_saveexec_b64 s[8:9], vcc
	s_cbranch_execz .LBB0_95
	v_mov_b32_e32 v0, 0
	global_load_dword v1, v0, s[10:11] offset:-256 sc1
	s_mov_b64 s[16:17], 0
	s_waitcnt vmcnt(0)
	v_cmp_lt_u32_e32 vcc, v1, v3
	s_and_saveexec_b64 s[14:15], vcc
	s_cbranch_execz .LBB0_94
	s_add_u32 s12, s26, 0x4200
	s_addc_u32 s13, s27, 0
	s_mov_b32 s0, 1
	s_branch .LBB0_87

.LBB0_89:
	global_load_dword v1, v0, s[10:11] offset:-256 sc1
	s_add_i32 s0, s0, 1
	s_mov_b64 s[20:21], -1
	s_waitcnt vmcnt(0)
	v_cmp_ge_u32_e32 vcc, v1, v3
	s_orn2_b64 s[28:29], vcc, exec
	s_branch .LBB0_86

.LBB0_95:
	s_or_b64 exec, exec, s[8:9]
	s_and_saveexec_b64 s[8:9], s[12:13]
	s_cbranch_execz .LBB0_97
.LBB0_97:
	s_or_b64 exec, exec, s[8:9]
	s_waitcnt vmcnt(0)
	buffer_inv sc1
	s_waitcnt vmcnt(0)

.LBB0_155:
	s_or_b64 exec, exec, s[8:9]
	s_and_saveexec_b64 s[8:9], s[12:13]
	s_cbranch_execz .LBB0_157
.LBB0_157:
	s_or_b64 exec, exec, s[8:9]
	s_waitcnt vmcnt(0)
	buffer_inv sc1
	s_waitcnt vmcnt(0)

.LBB0_214:
	s_or_b64 exec, exec, s[8:9]
	s_and_saveexec_b64 s[8:9], s[12:13]
	s_cbranch_execz .LBB0_216
.LBB0_216:
	s_or_b64 exec, exec, s[8:9]
	s_waitcnt vmcnt(0)
	buffer_inv sc1
	s_waitcnt vmcnt(0)

.LBB0_1139:
	s_or_b64 exec, exec, s[8:9]
	s_and_saveexec_b64 s[8:9], s[12:13]
	s_cbranch_execz .LBB0_1141
.LBB0_1141:
	s_or_b64 exec, exec, s[8:9]
	s_waitcnt vmcnt(0)
	buffer_inv sc1
	s_waitcnt vmcnt(0)

.LBB0_1203:
	s_or_b64 exec, exec, s[8:9]
	s_and_saveexec_b64 s[8:9], s[12:13]
	s_cbranch_execz .LBB0_1205
.LBB0_1205:
	s_or_b64 exec, exec, s[8:9]
	s_waitcnt vmcnt(0)
	buffer_inv sc1
	s_waitcnt vmcnt(0)

.LBB0_1337:
	s_or_b64 exec, exec, s[8:9]
	s_and_saveexec_b64 s[8:9], s[12:13]
	s_cbranch_execz .LBB0_1339
.LBB0_1339:
	s_or_b64 exec, exec, s[8:9]
	s_waitcnt vmcnt(0)
	buffer_inv sc1
	s_waitcnt vmcnt(0)

.LBB0_1407:
	s_or_b64 exec, exec, s[8:9]
	s_and_saveexec_b64 s[8:9], s[12:13]
	s_cbranch_execz .LBB0_1409
.LBB0_1409:
	s_or_b64 exec, exec, s[8:9]
	s_waitcnt vmcnt(0)
	buffer_inv sc1
	s_waitcnt vmcnt(0)

.LBB0_1508:
	s_or_b64 exec, exec, s[8:9]
	s_and_saveexec_b64 s[8:9], s[12:13]
	s_cbranch_execz .LBB0_1510
.LBB0_1510:
	s_or_b64 exec, exec, s[8:9]
	s_waitcnt vmcnt(0)
	buffer_inv sc1
	s_waitcnt vmcnt(0)

.LBB0_1634:
	s_or_b64 exec, exec, s[8:9]
	s_and_saveexec_b64 s[8:9], s[12:13]
	s_cbranch_execz .LBB0_1636
.LBB0_1636:
	s_or_b64 exec, exec, s[8:9]
	s_waitcnt vmcnt(0)
	buffer_inv sc1
	s_waitcnt vmcnt(0)

.LBB0_1743:
	s_or_b64 exec, exec, s[8:9]
	s_and_saveexec_b64 s[8:9], s[12:13]
	s_cbranch_execz .LBB0_1745
.LBB0_1745:
	s_or_b64 exec, exec, s[8:9]
	s_waitcnt vmcnt(0)
	buffer_inv sc1
	s_waitcnt vmcnt(0)

.LBB0_1996:
	s_or_b64 exec, exec, s[8:9]
	s_and_saveexec_b64 s[8:9], s[12:13]
	s_cbranch_execz .LBB0_1998
.LBB0_1998:
	s_or_b64 exec, exec, s[8:9]
	s_waitcnt vmcnt(0)
	buffer_inv sc1
	s_waitcnt vmcnt(0)

.LBB0_2249:
	s_or_b64 exec, exec, s[8:9]
	s_and_saveexec_b64 s[8:9], s[12:13]
	s_cbranch_execz .LBB0_2251
.LBB0_2251:
	s_or_b64 exec, exec, s[8:9]
	s_waitcnt vmcnt(0)
	buffer_inv sc1
	s_waitcnt vmcnt(0)

.LBB0_2336:
	s_or_b64 exec, exec, s[8:9]
	s_and_saveexec_b64 s[8:9], s[12:13]
	s_cbranch_execz .LBB0_2338
.LBB0_2338:
	s_or_b64 exec, exec, s[8:9]
	s_waitcnt vmcnt(0)
	buffer_inv sc1
	s_waitcnt vmcnt(0)

.LBB0_2421:
	s_or_b64 exec, exec, s[8:9]
	s_and_saveexec_b64 s[8:9], s[12:13]
	s_cbranch_execz .LBB0_2423
.LBB0_2423:
	s_or_b64 exec, exec, s[8:9]
	s_waitcnt vmcnt(0)
	buffer_inv sc1
	s_waitcnt vmcnt(0)
